# v69 + nt cache-policy hint on the final phase's once-read row loads and output stores
# speedup vs baseline: 1.0036x; 1.0036x over previous
.LBB0_1231:
	s_add_u32 s0, s82, s8
	s_addc_u32 s1, s83, s9
	global_load_dwordx2 v[32:33], v43, s[0:1]
	global_load_dwordx2 v[34:35], v144, s[0:1]
	s_add_u32 s0, s82, s16
	s_addc_u32 s1, s83, s17
	v_xor_b32_e32 v154, 16, v177
	v_xor_b32_e32 v155, 32, v177
	s_add_u32 s8, s8, 16
	s_addc_u32 s9, s9, 0
	s_add_i32 s5, s5, 2
	s_waitcnt vmcnt(0)
	v_ashrrev_i32_e32 v49, 31, v32
	v_mov_b32_e32 v48, v32
	v_lshlrev_b64 v[52:53], 11, v[48:49]
	v_lshl_add_u64 v[86:87], v[40:41], 0, v[52:53]
	global_load_dwordx2 v[52:53], v[86:87], off nt
	global_load_dwordx2 v[58:59], v[86:87], off offset:512 nt
	global_load_dwordx2 v[76:77], v[86:87], off offset:1024 nt
	global_load_dwordx2 v[90:91], v[86:87], off offset:1536 nt
	v_ashrrev_i32_e32 v49, 31, v33
	v_mov_b32_e32 v48, v33
	v_lshlrev_b64 v[32:33], 11, v[48:49]
	v_lshl_add_u64 v[48:49], s[82:83], 0, v[44:45]
	v_add_co_u32_e32 v74, vcc, s2, v48
	v_lshl_add_u64 v[32:33], v[40:41], 0, v[32:33]
	s_nop 0
	v_addc_co_u32_e32 v75, vcc, 0, v49, vcc
	global_load_dwordx2 v[50:51], v[74:75], off nt
	global_load_dwordx2 v[80:81], v[32:33], off offset:1024 nt
	global_load_dwordx2 v[54:55], v[74:75], off offset:512 nt
	global_load_dwordx2 v[62:63], v[74:75], off offset:1024 nt
	v_lshl_add_u64 v[44:45], v[44:45], 0, s[6:7]
	s_waitcnt vmcnt(7)
	v_lshlrev_b32_e32 v56, 16, v52
	v_and_b32_e32 v57, 0xffff0000, v52
	v_lshlrev_b32_e32 v60, 16, v53
	v_and_b32_e32 v61, 0xffff0000, v53
	global_load_dwordx2 v[52:53], v[32:33], off nt
	s_waitcnt vmcnt(7)
	v_lshlrev_b32_e32 v64, 16, v58
	v_and_b32_e32 v65, 0xffff0000, v58
	v_lshlrev_b32_e32 v66, 16, v59
	v_and_b32_e32 v67, 0xffff0000, v59
	global_load_dwordx2 v[58:59], v[32:33], off offset:512 nt
	s_waitcnt vmcnt(7)
	v_lshlrev_b32_e32 v70, 16, v76
	v_and_b32_e32 v71, 0xffff0000, v76
	v_lshlrev_b32_e32 v76, 16, v77
	s_waitcnt vmcnt(5)
	v_lshlrev_b32_e32 v48, 16, v50
	v_and_b32_e32 v49, 0xffff0000, v50
	v_lshlrev_b32_e32 v50, 16, v51
	v_and_b32_e32 v51, 0xffff0000, v51
	v_and_b32_e32 v77, 0xffff0000, v77
	v_lshlrev_b32_e32 v86, 16, v90
	v_and_b32_e32 v87, 0xffff0000, v90
	v_lshlrev_b32_e32 v90, 16, v91
	v_and_b32_e32 v91, 0xffff0000, v91
	s_waitcnt vmcnt(4)
	v_lshlrev_b32_e32 v84, 16, v80
	v_and_b32_e32 v85, 0xffff0000, v80
	v_lshlrev_b32_e32 v88, 16, v81
	v_and_b32_e32 v89, 0xffff0000, v81
	global_load_dwordx2 v[80:81], v[74:75], off offset:1536 nt
	s_waitcnt vmcnt(2)
	v_lshlrev_b32_e32 v68, 16, v52
	global_load_dwordx2 v[32:33], v[32:33], off offset:1536 nt
	v_and_b32_e32 v69, 0xffff0000, v52
	v_lshlrev_b32_e32 v72, 16, v53
	v_and_b32_e32 v73, 0xffff0000, v53
	v_pk_mul_f32 v[68:69], v[34:35], v[68:69] op_sel:[1,0]
	v_pk_mul_f32 v[72:73], v[34:35], v[72:73] op_sel:[1,0]
	v_pk_fma_f32 v[56:57], v[34:35], v[56:57], v[68:69] op_sel_hi:[0,1,1]
	v_pk_fma_f32 v[72:73], v[34:35], v[60:61], v[72:73] op_sel_hi:[0,1,1]
	v_pk_fma_f32 v[60:61], v[16:17], v[56:57], v[48:49]
	v_pk_fma_f32 v[68:69], v[18:19], v[72:73], v[50:51]
	v_pk_mul_f32 v[50:51], v[60:61], v[60:61]
	v_pk_mul_f32 v[48:49], v[68:69], v[68:69]
	s_waitcnt vmcnt(2)
	v_lshlrev_b32_e32 v78, 16, v58
	v_and_b32_e32 v79, 0xffff0000, v58
	v_lshlrev_b32_e32 v82, 16, v59
	v_and_b32_e32 v83, 0xffff0000, v59
	v_pk_mov_b32 v[56:57], v[50:51], v[48:49] op_sel:[1,0]
	v_mov_b32_e32 v51, v49
	v_pk_add_f32 v[48:49], v[56:57], v[50:51]
	v_pk_mul_f32 v[50:51], v[34:35], v[78:79] op_sel:[1,0]
	v_pk_mul_f32 v[56:57], v[34:35], v[82:83] op_sel:[1,0]
	v_lshlrev_b32_e32 v52, 16, v54
	v_and_b32_e32 v53, 0xffff0000, v54
	v_lshlrev_b32_e32 v54, 16, v55
	v_and_b32_e32 v55, 0xffff0000, v55
	v_pk_fma_f32 v[56:57], v[34:35], v[66:67], v[56:57] op_sel_hi:[0,1,1]
	v_pk_fma_f32 v[50:51], v[34:35], v[64:65], v[50:51] op_sel_hi:[0,1,1]
	v_pk_fma_f32 v[64:65], v[20:21], v[50:51], v[52:53]
	v_pk_fma_f32 v[66:67], v[22:23], v[56:57], v[54:55]
	v_pk_mul_f32 v[52:53], v[64:65], v[64:65]
	v_pk_mul_f32 v[50:51], v[66:67], v[66:67]
	v_lshlrev_b32_e32 v58, 16, v62
	v_pk_mov_b32 v[54:55], v[52:53], v[50:51] op_sel:[1,0]
	v_mov_b32_e32 v53, v51
	v_pk_add_f32 v[50:51], v[54:55], v[52:53]
	v_pk_mul_f32 v[54:55], v[34:35], v[84:85] op_sel:[1,0]
	v_and_b32_e32 v59, 0xffff0000, v62
	v_pk_fma_f32 v[54:55], v[34:35], v[70:71], v[54:55] op_sel_hi:[0,1,1]
	v_pk_mul_f32 v[52:53], v[34:35], v[88:89] op_sel:[1,0]
	v_pk_fma_f32 v[70:71], v[24:25], v[54:55], v[58:59]
	v_lshlrev_b32_e32 v62, 16, v63
	v_and_b32_e32 v63, 0xffff0000, v63
	v_pk_fma_f32 v[52:53], v[34:35], v[76:77], v[52:53] op_sel_hi:[0,1,1]
	v_pk_fma_f32 v[62:63], v[26:27], v[52:53], v[62:63]
	v_pk_add_f32 v[48:49], v[48:49], v[48:49] op_sel:[0,1] op_sel_hi:[1,0]
	v_pk_add_f32 v[50:51], v[50:51], v[50:51] op_sel:[0,1] op_sel_hi:[1,0]
	v_lshl_add_u64 v[78:79], s[10:11], 0, v[36:37]
	s_add_u32 s10, s10, 0x2000
	s_addc_u32 s11, s11, 0
	s_add_u32 s16, s16, 16
	s_addc_u32 s17, s17, 0
	s_waitcnt vmcnt(1)
	v_lshlrev_b32_e32 v74, 16, v80
	v_and_b32_e32 v75, 0xffff0000, v80
	v_lshlrev_b32_e32 v80, 16, v81
	v_and_b32_e32 v81, 0xffff0000, v81
	s_waitcnt vmcnt(0)
	v_lshlrev_b32_e32 v92, 16, v32
	v_and_b32_e32 v93, 0xffff0000, v32
	v_lshlrev_b32_e32 v94, 16, v33
	v_and_b32_e32 v95, 0xffff0000, v33
	global_load_dwordx2 v[96:97], v43, s[0:1]
	global_load_dwordx2 v[32:33], v144, s[0:1]
	v_pk_mul_f32 v[54:55], v[34:35], v[92:93] op_sel:[1,0]
	v_pk_mul_f32 v[52:53], v[34:35], v[94:95] op_sel:[1,0]
	v_pk_fma_f32 v[54:55], v[34:35], v[86:87], v[54:55] op_sel_hi:[0,1,1]
	v_pk_fma_f32 v[72:73], v[28:29], v[54:55], v[74:75]
	v_pk_fma_f32 v[34:35], v[34:35], v[90:91], v[52:53] op_sel_hi:[0,1,1]
	v_mul_f32_e32 v52, v72, v72
	v_mul_f32_e32 v53, v73, v73
	v_mov_b32_e32 v49, v52
	v_mov_b32_e32 v51, v53
	v_pk_fma_f32 v[34:35], v[30:31], v[34:35], v[80:81]
	v_pk_add_f32 v[48:49], v[48:49], v[50:51]
	v_mul_f32_e32 v50, v71, v71
	v_mul_f32_e32 v52, v63, v63
	v_mul_f32_e32 v54, v34, v34
	v_mul_f32_e32 v55, v35, v35
	v_pk_fma_f32 v[50:51], v[70:71], v[70:71], v[50:51] op_sel_hi:[1,1,0]
	v_pk_fma_f32 v[52:53], v[62:63], v[62:63], v[52:53] op_sel_hi:[1,1,0]
	v_mov_b32_e32 v51, v54
	v_mov_b32_e32 v53, v55
	v_pk_add_f32 v[50:51], v[50:51], v[52:53]
	s_mov_b32 s0, 0x3a800000
	v_pk_add_f32 v[74:75], v[48:49], v[50:51]
	s_waitcnt vmcnt(1)
	v_ashrrev_i32_e32 v99, 31, v96
	v_mov_b32_e32 v98, v96
	v_lshlrev_b64 v[102:103], 11, v[98:99]
	v_lshl_add_u64 v[134:135], v[40:41], 0, v[102:103]
	global_load_dwordx2 v[102:103], v[134:135], off nt
	global_load_dwordx2 v[106:107], v[134:135], off offset:512 nt
	global_load_dwordx2 v[124:125], v[134:135], off offset:1024 nt
	global_load_dwordx2 v[138:139], v[134:135], off offset:1536 nt
	v_ashrrev_i32_e32 v99, 31, v97
	v_mov_b32_e32 v98, v97
	v_lshlrev_b64 v[100:101], 11, v[98:99]
	v_lshl_add_u64 v[140:141], v[40:41], 0, v[100:101]
	global_load_dwordx2 v[100:101], v[140:141], off nt
	global_load_dwordx2 v[128:129], v[140:141], off offset:1024 nt
	global_load_dwordx2 v[142:143], v[140:141], off offset:1536 nt
	v_lshl_add_u64 v[96:97], s[82:83], 0, v[46:47]
	v_add_co_u32_e32 v122, vcc, s2, v96
	v_lshl_add_u64 v[46:47], v[46:47], 0, s[6:7]
	s_nop 0
	v_addc_co_u32_e32 v123, vcc, 0, v97, vcc
	global_load_dwordx2 v[98:99], v[122:123], off nt
	global_load_dwordx2 v[110:111], v[122:123], off offset:1024 nt
	v_cmp_lt_i32_e32 vcc, v146, v145
	s_waitcnt vmcnt(8)
	v_lshlrev_b32_e32 v104, 16, v102
	s_waitcnt vmcnt(7)
	v_lshlrev_b32_e32 v112, 16, v106
	v_and_b32_e32 v113, 0xffff0000, v106
	v_lshlrev_b32_e32 v114, 16, v107
	v_and_b32_e32 v115, 0xffff0000, v107
	global_load_dwordx2 v[106:107], v[140:141], off offset:512 nt
	v_and_b32_e32 v105, 0xffff0000, v102
	v_lshlrev_b32_e32 v108, 16, v103
	v_and_b32_e32 v109, 0xffff0000, v103
	global_load_dwordx2 v[102:103], v[122:123], off offset:512 nt
	s_waitcnt vmcnt(6)
	v_lshlrev_b32_e32 v116, 16, v100
	v_and_b32_e32 v117, 0xffff0000, v100
	v_lshlrev_b32_e32 v120, 16, v101
	v_and_b32_e32 v121, 0xffff0000, v101
	v_pk_mul_f32 v[48:49], v[32:33], v[116:117] op_sel:[1,0]
	v_pk_mul_f32 v[50:51], v[32:33], v[120:121] op_sel:[1,0]
	v_pk_fma_f32 v[48:49], v[32:33], v[104:105], v[48:49] op_sel_hi:[0,1,1]
	v_pk_fma_f32 v[50:51], v[32:33], v[108:109], v[50:51] op_sel_hi:[0,1,1]
	v_lshlrev_b32_e32 v118, 16, v124
	v_and_b32_e32 v119, 0xffff0000, v124
	v_lshlrev_b32_e32 v134, 16, v138
	v_and_b32_e32 v135, 0xffff0000, v138
	v_lshlrev_b32_e32 v124, 16, v125
	v_and_b32_e32 v125, 0xffff0000, v125
	v_lshlrev_b32_e32 v138, 16, v139
	v_and_b32_e32 v139, 0xffff0000, v139
	v_cndmask_b32_e32 v150, v177, v146, vcc
	v_lshlrev_b32_e32 v150, 2, v150
	v_cmp_lt_i32_e32 vcc, v147, v145
	s_waitcnt vmcnt(5)
	v_lshlrev_b32_e32 v132, 16, v128
	v_and_b32_e32 v133, 0xffff0000, v128
	v_lshlrev_b32_e32 v136, 16, v129
	v_and_b32_e32 v137, 0xffff0000, v129
	global_load_dwordx2 v[128:129], v[122:123], off offset:1536 nt
	s_waitcnt vmcnt(4)
	v_lshlrev_b32_e32 v96, 16, v98
	v_and_b32_e32 v97, 0xffff0000, v98
	v_lshlrev_b32_e32 v98, 16, v99
	v_and_b32_e32 v99, 0xffff0000, v99
	v_lshlrev_b32_e32 v140, 16, v142
	v_and_b32_e32 v141, 0xffff0000, v142
	v_lshlrev_b32_e32 v142, 16, v143
	v_and_b32_e32 v143, 0xffff0000, v143
	v_cndmask_b32_e32 v151, v177, v147, vcc
	v_lshlrev_b32_e32 v151, 2, v151
	v_cmp_lt_i32_e32 vcc, v148, v145
	v_pk_fma_f32 v[80:81], v[16:17], v[48:49], v[96:97]
	v_pk_fma_f32 v[82:83], v[18:19], v[50:51], v[98:99]
	v_pk_mul_f32 v[58:59], v[32:33], v[140:141] op_sel:[1,0]
	v_cndmask_b32_e32 v152, v177, v148, vcc
	v_lshlrev_b32_e32 v152, 2, v152
	v_cmp_lt_i32_e32 vcc, v149, v145
	v_pk_mul_f32 v[48:49], v[82:83], v[82:83]
	v_pk_mul_f32 v[50:51], v[80:81], v[80:81]
	v_pk_fma_f32 v[58:59], v[32:33], v[134:135], v[58:59] op_sel_hi:[0,1,1]
	v_cndmask_b32_e32 v153, v177, v149, vcc
	v_lshlrev_b32_e32 v153, 2, v153
	v_cmp_lt_i32_e32 vcc, v154, v145
	v_pk_mov_b32 v[52:53], v[50:51], v[48:49] op_sel:[1,0]
	v_mov_b32_e32 v51, v49
	v_cndmask_b32_e32 v154, v177, v154, vcc
	v_lshlrev_b32_e32 v154, 2, v154
	v_cmp_lt_i32_e32 vcc, v155, v145
	v_pk_add_f32 v[76:77], v[52:53], v[50:51]
	s_waitcnt vmcnt(2)
	v_lshlrev_b32_e32 v126, 16, v106
	v_and_b32_e32 v127, 0xffff0000, v106
	v_lshlrev_b32_e32 v130, 16, v107
	v_and_b32_e32 v131, 0xffff0000, v107
	v_pk_mul_f32 v[48:49], v[32:33], v[126:127] op_sel:[1,0]
	v_pk_mul_f32 v[50:51], v[32:33], v[130:131] op_sel:[1,0]
	s_waitcnt vmcnt(1)
	v_lshlrev_b32_e32 v100, 16, v102
	v_and_b32_e32 v101, 0xffff0000, v102
	v_lshlrev_b32_e32 v102, 16, v103
	v_and_b32_e32 v103, 0xffff0000, v103
	v_pk_fma_f32 v[50:51], v[32:33], v[114:115], v[50:51] op_sel_hi:[0,1,1]
	v_pk_fma_f32 v[48:49], v[32:33], v[112:113], v[48:49] op_sel_hi:[0,1,1]
	v_pk_fma_f32 v[48:49], v[20:21], v[48:49], v[100:101]
	v_pk_fma_f32 v[50:51], v[22:23], v[50:51], v[102:103]
	v_pk_mul_f32 v[54:55], v[48:49], v[48:49]
	v_pk_mul_f32 v[52:53], v[50:51], v[50:51]
	v_lshlrev_b32_e32 v106, 16, v110
	v_pk_mov_b32 v[56:57], v[54:55], v[52:53] op_sel:[1,0]
	v_mov_b32_e32 v55, v53
	v_pk_add_f32 v[84:85], v[56:57], v[54:55]
	v_pk_mul_f32 v[54:55], v[32:33], v[132:133] op_sel:[1,0]
	v_and_b32_e32 v107, 0xffff0000, v110
	v_pk_fma_f32 v[54:55], v[32:33], v[118:119], v[54:55] op_sel_hi:[0,1,1]
	v_pk_mul_f32 v[52:53], v[32:33], v[136:137] op_sel:[1,0]
	v_pk_fma_f32 v[56:57], v[24:25], v[54:55], v[106:107]
	v_pk_mul_f32 v[54:55], v[32:33], v[142:143] op_sel:[1,0]
	v_pk_fma_f32 v[52:53], v[32:33], v[124:125], v[52:53] op_sel_hi:[0,1,1]
	v_pk_fma_f32 v[32:33], v[32:33], v[138:139], v[54:55] op_sel_hi:[0,1,1]
	v_lshlrev_b32_e32 v110, 16, v111
	v_and_b32_e32 v111, 0xffff0000, v111
	v_pk_fma_f32 v[52:53], v[26:27], v[52:53], v[110:111]
	v_cndmask_b32_e32 v155, v177, v155, vcc
	v_lshlrev_b32_e32 v155, 2, v155
	s_waitcnt vmcnt(0)
	v_lshlrev_b32_e32 v122, 16, v128
	v_and_b32_e32 v123, 0xffff0000, v128
	v_lshlrev_b32_e32 v128, 16, v129
	v_and_b32_e32 v129, 0xffff0000, v129
	v_pk_fma_f32 v[58:59], v[28:29], v[58:59], v[122:123]
	v_pk_fma_f32 v[54:55], v[30:31], v[32:33], v[128:129]
	v_pk_add_f32 v[32:33], v[76:77], v[76:77] op_sel:[0,1] op_sel_hi:[1,0]
	v_pk_add_f32 v[76:77], v[84:85], v[84:85] op_sel:[0,1] op_sel_hi:[1,0]
	v_mul_f32_e32 v84, v53, v53
	v_mul_f32_e32 v86, v58, v58
	v_mul_f32_e32 v87, v59, v59
	v_mul_f32_e32 v88, v54, v54
	v_mul_f32_e32 v89, v55, v55
	v_pk_fma_f32 v[84:85], v[52:53], v[52:53], v[84:85] op_sel_hi:[1,1,0]
	v_mov_b32_e32 v33, v86
	v_mov_b32_e32 v77, v87
	v_mov_b32_e32 v85, v89
	v_pk_add_f32 v[32:33], v[32:33], v[76:77]
	v_mul_f32_e32 v76, v57, v57
	v_pk_fma_f32 v[76:77], v[56:57], v[56:57], v[76:77] op_sel_hi:[1,1,0]
	s_nop 0
	v_mov_b32_e32 v77, v88
	v_pk_add_f32 v[76:77], v[76:77], v[84:85]
	s_nop 0
	v_pk_add_f32 v[32:33], v[32:33], v[76:77]
	v_mov_b32_e32 v77, v74
	v_mov_b32_e32 v76, v32
	v_mov_b32_e32 v74, v33
	v_pk_add_f32 v[32:33], v[76:77], v[74:75]
	ds_bpermute_b32 v75, v150, v33
	ds_bpermute_b32 v74, v150, v32
	s_waitcnt lgkmcnt(0)
	v_pk_add_f32 v[32:33], v[32:33], v[74:75]
	ds_bpermute_b32 v75, v151, v33
	ds_bpermute_b32 v74, v151, v32
	s_waitcnt lgkmcnt(0)
	v_pk_add_f32 v[32:33], v[32:33], v[74:75]
	ds_bpermute_b32 v75, v152, v33
	ds_bpermute_b32 v74, v152, v32
	s_waitcnt lgkmcnt(0)
	v_pk_add_f32 v[32:33], v[32:33], v[74:75]
	ds_bpermute_b32 v75, v153, v33
	ds_bpermute_b32 v74, v153, v32
	s_waitcnt lgkmcnt(0)
	v_pk_add_f32 v[32:33], v[32:33], v[74:75]
	ds_bpermute_b32 v75, v154, v33
	ds_bpermute_b32 v74, v154, v32
	s_waitcnt lgkmcnt(0)
	v_pk_add_f32 v[32:33], v[32:33], v[74:75]
	ds_bpermute_b32 v75, v155, v33
	ds_bpermute_b32 v74, v155, v32
	s_waitcnt lgkmcnt(0)
	v_pk_add_f32 v[32:33], v[32:33], v[74:75]
	s_nop 0
	v_pk_fma_f32 v[84:85], v[32:33], s[0:1], v[42:43] op_sel_hi:[1,0,0]
	s_nop 0
	v_mul_f32_e32 v32, 0x4b800000, v85
	v_cmp_gt_f32_e64 s[0:1], s3, v85
	v_cmp_gt_f32_e32 vcc, s3, v84
	s_nop 0
	v_cndmask_b32_e64 v32, v85, v32, s[0:1]
	v_rsq_f32_e32 v32, v32
	s_nop 0
	v_mul_f32_e32 v33, 0x45800000, v32
	v_cndmask_b32_e64 v32, v32, v33, s[0:1]
	v_pk_mul_f32 v[60:61], v[60:61], v[32:33] op_sel_hi:[1,0]
	v_pk_mul_f32 v[62:63], v[62:63], v[32:33] op_sel_hi:[1,0]
	v_pk_mul_f32 v[68:69], v[68:69], v[32:33] op_sel_hi:[1,0]
	v_pk_mul_f32 v[74:75], v[0:1], v[60:61]
	v_pk_mul_f32 v[60:61], v[64:65], v[32:33] op_sel_hi:[1,0]
	v_pk_mul_f32 v[64:65], v[66:67], v[32:33] op_sel_hi:[1,0]
	v_pk_mul_f32 v[62:63], v[10:11], v[62:63]
	v_pk_mul_f32 v[66:67], v[6:7], v[64:65]
	v_pk_mul_f32 v[64:65], v[4:5], v[60:61]
	v_pk_mul_f32 v[60:61], v[70:71], v[32:33] op_sel_hi:[1,0]
	global_store_dwordx4 v[78:79], v[64:67], off offset:1024 nt
	v_pk_mul_f32 v[60:61], v[8:9], v[60:61]
	global_store_dwordx4 v[78:79], v[60:63], off offset:2048 nt
	v_pk_mul_f32 v[76:77], v[2:3], v[68:69]
	global_store_dwordx4 v[78:79], v[74:77], off nt
	v_pk_mul_f32 v[60:61], v[72:73], v[32:33] op_sel_hi:[1,0]
	v_pk_mul_f32 v[32:33], v[34:35], v[32:33] op_sel_hi:[1,0]
	v_lshl_add_u64 v[62:63], s[18:19], 0, v[36:37]
	v_pk_mul_f32 v[34:35], v[14:15], v[32:33]
	v_pk_mul_f32 v[32:33], v[12:13], v[60:61]
	global_store_dwordx4 v[78:79], v[32:35], off offset:3072 nt
	s_add_u32 s18, s18, 0x2000
	s_addc_u32 s19, s19, 0
	v_mul_f32_e32 v32, 0x4b800000, v84
	v_cndmask_b32_e32 v32, v84, v32, vcc
	v_rsq_f32_e32 v32, v32
	s_cmp_gt_u32 s5, 29
	v_mul_f32_e32 v33, 0x45800000, v32
	v_cndmask_b32_e32 v60, v32, v33, vcc
	v_pk_mul_f32 v[32:33], v[80:81], v[60:61] op_sel_hi:[1,0]
	v_pk_mul_f32 v[34:35], v[82:83], v[60:61] op_sel_hi:[1,0]
	v_pk_mul_f32 v[32:33], v[0:1], v[32:33]
	v_pk_mul_f32 v[34:35], v[2:3], v[34:35]
	global_store_dwordx4 v[62:63], v[32:35], off nt
	s_nop 1
	v_pk_mul_f32 v[32:33], v[48:49], v[60:61] op_sel_hi:[1,0]
	v_pk_mul_f32 v[34:35], v[50:51], v[60:61] op_sel_hi:[1,0]
	v_pk_mul_f32 v[32:33], v[4:5], v[32:33]
	v_pk_mul_f32 v[34:35], v[6:7], v[34:35]
	global_store_dwordx4 v[62:63], v[32:35], off offset:1024 nt
	s_nop 1
	v_pk_mul_f32 v[32:33], v[56:57], v[60:61] op_sel_hi:[1,0]
	v_pk_mul_f32 v[34:35], v[52:53], v[60:61] op_sel_hi:[1,0]
	v_pk_mul_f32 v[32:33], v[8:9], v[32:33]
	v_pk_mul_f32 v[34:35], v[10:11], v[34:35]
	global_store_dwordx4 v[62:63], v[32:35], off offset:2048 nt
	s_nop 1
	v_pk_mul_f32 v[32:33], v[58:59], v[60:61] op_sel_hi:[1,0]
	v_pk_mul_f32 v[34:35], v[54:55], v[60:61] op_sel_hi:[1,0]
	v_pk_mul_f32 v[32:33], v[12:13], v[32:33]
	v_pk_mul_f32 v[34:35], v[14:15], v[34:35]
	global_store_dwordx4 v[62:63], v[32:35], off offset:3072 nt
	s_cbranch_scc0 .LBB0_1231
	s_add_i32 s67, s67, s95
	s_add_i32 s20, s20, s89
	s_add_i32 s4, s4, s89
	s_cmpk_gt_i32 s67, 0xff
	s_cbranch_scc0 .LBB0_1230
